# block-major join trimmed: one ring-slot address with immediate offsets for the pair's second block, wait count picked by two nested tests instead of arithmetic on the state
# speedup vs baseline: 1.0168x; 1.0046x over previous
.Lbm_g2_end_nb:
.Lbm_join:
	s_add_i32 s10, s1, 0x4000
	s_and_b32 s10, s10, 0x4000
	v_add_u32_e32 v78, s10, v188
	s_cmp_ge_u32 s99, 2
	s_cbranch_scc0 .Lbm_jb0
	s_cmp_eq_u32 s99, 4
	s_cbranch_scc1 .Lbm_jb0
	s_cmp_lt_i32 s100, 0
	s_cbranch_scc1 .Lbm_jw4
	s_waitcnt vmcnt(6)
	s_branch .Lbm_jwd

.Lbm_jb0:
	s_cmp_lt_i32 s100, 0
	s_cbranch_scc1 .Lbm_jw0
	s_waitcnt vmcnt(2)
	s_branch .Lbm_jwd

; #define LAS __attribute__((address_space(3)))
; __device__ __forceinline__ void stage_load(Stage& s, const unsigned char* kg, size_t kstride, const unsigned char* vg, size_t vstride, int tid, bool hasv) {
;     const int row = tid >> 3, ch = tid & 7;
;     s.k = *(const u32x4*)(kg + (size_t)row * kstride + ch * 16);
;     if (hasv) s.v = *(const u32x4*)(vg + (size_t)row * vstride + ch * 16);
; }
; __device__ __forceinline__ void stage_store(const Stage& s, LAS unsigned char* lds, int buf, int tid, bool hasv) {
;     const int row = tid >> 3, ch = tid & 7, off = row * 128 + ((ch ^ (row & 7)) << 4);
;     *(LAS u32x4*)(lds + NSA_KB + buf * 8192 + off) = s.k;
;     if (hasv) *(LAS u32x4*)(lds + NSA_VB + buf * 8192 + off) = s.v;
; }
.Lbm_jwd:
	s_cmp_ge_u32 s99, 3
	s_cbranch_scc1 .Lbm_jB
	ds_write_b128 v78, v[26:29]
	ds_write_b128 v78, v[22:25] offset:32768
	ds_write_b128 v78, v[30:33] offset:8192
	ds_write_b128 v78, v[34:37] offset:40960
	s_add_i32 s10, s26, -4
	s_cmp_eq_u32 s99, 2
	s_cbranch_scc1 .Lbm_jA2
	s_mov_b32 s99, 0
	s_mov_b32 s101, 4
	s_add_i32 s11, s75, 2
	s_cmp_le_i32 s11, s26
	s_cbranch_scc1 .Lbm_jA1
	s_lshl_b32 s11, s91, 3
	v_add_u32_e32 v82, s11, v184
	v_lshlrev_b32_e32 v82, 11, v82
	v_mov_b32_e32 v83, 0
	v_lshl_add_u64 v[82:83], v[82:83], 0, v[246:247]
	v_add_co_u32_e32 v254, vcc, 0x2000, v82
	s_nop 1
	v_addc_co_u32_e32 v255, vcc, 0, v83, vcc
	global_load_dwordx4 v[6:9], v[82:83], off
	global_load_dwordx4 v[10:13], v[82:83], off offset:64
	global_load_dwordx4 v[14:17], v[254:255], off
	global_load_dwordx4 v[18:21], v[254:255], off offset:64

; #define LAS __attribute__((address_space(3)))
; __device__ __forceinline__ void stage_load(Stage& s, const unsigned char* kg, size_t kstride, const unsigned char* vg, size_t vstride, int tid, bool hasv) {
;     const int row = tid >> 3, ch = tid & 7;
;     s.k = *(const u32x4*)(kg + (size_t)row * kstride + ch * 16);
;     if (hasv) s.v = *(const u32x4*)(vg + (size_t)row * vstride + ch * 16);
; }
; __device__ __forceinline__ void stage_store(const Stage& s, LAS unsigned char* lds, int buf, int tid, bool hasv) {
;     const int row = tid >> 3, ch = tid & 7, off = row * 128 + ((ch ^ (row & 7)) << 4);
;     *(LAS u32x4*)(lds + NSA_KB + buf * 8192 + off) = s.k;
;     if (hasv) *(LAS u32x4*)(lds + NSA_VB + buf * 8192 + off) = s.v;
; }
.Lbm_jB:
	ds_write_b128 v78, v[10:13]
	ds_write_b128 v78, v[6:9] offset:32768
	ds_write_b128 v78, v[14:17] offset:8192
	ds_write_b128 v78, v[18:21] offset:40960
	s_add_i32 s10, s26, -4
	s_cmp_eq_u32 s99, 3
	s_cbranch_scc1 .Lbm_jB3
	s_mov_b32 s99, 0
	s_mov_b32 s101, 4
	s_add_i32 s11, s75, 2
	s_cmp_le_i32 s11, s26
	s_cbranch_scc1 .Lbm_jB1
	s_lshl_b32 s11, s91, 3
	v_add_u32_e32 v82, s11, v184
	v_lshlrev_b32_e32 v82, 11, v82
	v_mov_b32_e32 v83, 0
	v_lshl_add_u64 v[82:83], v[82:83], 0, v[246:247]
	v_add_co_u32_e32 v254, vcc, 0x2000, v82
	s_nop 1
	v_addc_co_u32_e32 v255, vcc, 0, v83, vcc
	global_load_dwordx4 v[6:9], v[82:83], off
	global_load_dwordx4 v[10:13], v[82:83], off offset:64
	global_load_dwordx4 v[14:17], v[254:255], off
	global_load_dwordx4 v[18:21], v[254:255], off offset:64
